# v53 + NA loop: the 32 default -1e30 moves of a local tile run only when the tile is outside the wave's window
# speedup vs baseline: 1.0031x; 1.0031x over previous
.LBB0_818:
	s_ashr_i32 s3, s2, 31
	s_mul_hi_u32 s10, s2, s62
	s_mul_i32 s3, s3, s62
	s_add_i32 s3, s10, s3
	s_mul_i32 s2, s2, s62
	s_lshl_b64 s[2:3], s[2:3], 1
	s_add_u32 s10, s8, s2
	s_addc_u32 s11, s9, s3
	s_add_u32 s2, s6, s2
	s_addc_u32 s3, s7, s3
	global_load_dwordx4 v[146:149], v128, s[10:11]
	global_load_dwordx4 v[150:153], v178, s[10:11]
	global_load_dwordx4 v[154:157], v128, s[2:3]
	global_load_dwordx4 v[158:161], v178, s[2:3]
	ds_read_b64_tr_b16 v[212:213], v186 offset:0
	ds_read_b64_tr_b16 v[214:215], v186 offset:0x800
	ds_read_b64_tr_b16 v[216:217], v186 offset:0x1000
	ds_read_b64_tr_b16 v[218:219], v186 offset:0x1800
	ds_read_b64_tr_b16 v[220:221], v186 offset:0x2000
	ds_read_b64_tr_b16 v[222:223], v186 offset:0x2800
	ds_read_b64_tr_b16 v[224:225], v186 offset:0x3000
	ds_read_b64_tr_b16 v[226:227], v186 offset:0x3800
	s_waitcnt lgkmcnt(0)
	s_cmp_lt_u32 s24, 4
	v_mfma_f32_32x32x16_bf16 v[48:63], v[212:215], v[162:165], v[48:63]
	ds_read_b64_tr_b16 v[212:213], v186 offset:0x200
	ds_read_b64_tr_b16 v[214:215], v186 offset:0xa00
	v_mfma_f32_32x32x16_bf16 v[48:63], v[216:219], v[166:169], v[48:63]
	ds_read_b64_tr_b16 v[216:217], v186 offset:0x1200
	ds_read_b64_tr_b16 v[218:219], v186 offset:0x1a00
	v_mfma_f32_32x32x16_bf16 v[48:63], v[220:223], v[170:173], v[48:63]
	ds_read_b64_tr_b16 v[220:221], v186 offset:0x2200
	ds_read_b64_tr_b16 v[222:223], v186 offset:0x2a00
	v_mfma_f32_32x32x16_bf16 v[48:63], v[224:227], v[174:177], v[48:63]
	ds_read_b64_tr_b16 v[224:225], v186 offset:0x3200
	ds_read_b64_tr_b16 v[226:227], v186 offset:0x3a00
	s_waitcnt lgkmcnt(0)
	v_mfma_f32_32x32x16_bf16 v[32:47], v[212:215], v[162:165], v[32:47]
	ds_read_b64_tr_b16 v[212:213], v186 offset:0x400
	ds_read_b64_tr_b16 v[214:215], v186 offset:0xc00
	v_mfma_f32_32x32x16_bf16 v[32:47], v[216:219], v[166:169], v[32:47]
	ds_read_b64_tr_b16 v[216:217], v186 offset:0x1400
	ds_read_b64_tr_b16 v[218:219], v186 offset:0x1c00
	v_mfma_f32_32x32x16_bf16 v[32:47], v[220:223], v[170:173], v[32:47]
	ds_read_b64_tr_b16 v[220:221], v186 offset:0x2400
	ds_read_b64_tr_b16 v[222:223], v186 offset:0x2c00
	v_mfma_f32_32x32x16_bf16 v[32:47], v[224:227], v[174:177], v[32:47]
	ds_read_b64_tr_b16 v[224:225], v186 offset:0x3400
	ds_read_b64_tr_b16 v[226:227], v186 offset:0x3c00
	s_waitcnt lgkmcnt(0)
	v_mfma_f32_32x32x16_bf16 v[16:31], v[212:215], v[162:165], v[16:31]
	ds_read_b64_tr_b16 v[212:213], v186 offset:0x600
	ds_read_b64_tr_b16 v[214:215], v186 offset:0xe00
	v_mfma_f32_32x32x16_bf16 v[16:31], v[216:219], v[166:169], v[16:31]
	ds_read_b64_tr_b16 v[216:217], v186 offset:0x1600
	ds_read_b64_tr_b16 v[218:219], v186 offset:0x1e00
	v_mfma_f32_32x32x16_bf16 v[16:31], v[220:223], v[170:173], v[16:31]
	ds_read_b64_tr_b16 v[220:221], v186 offset:0x2600
	ds_read_b64_tr_b16 v[222:223], v186 offset:0x2e00
	v_mfma_f32_32x32x16_bf16 v[16:31], v[224:227], v[174:177], v[16:31]
	ds_read_b64_tr_b16 v[224:225], v186 offset:0x3600
	ds_read_b64_tr_b16 v[226:227], v186 offset:0x3e00
	s_waitcnt lgkmcnt(0)
	v_mfma_f32_32x32x16_bf16 v[0:15], v[212:215], v[162:165], v[0:15]
	v_mfma_f32_32x32x16_bf16 v[0:15], v[216:219], v[166:169], v[0:15]
	v_mfma_f32_32x32x16_bf16 v[0:15], v[220:223], v[170:173], v[0:15]
	v_mfma_f32_32x32x16_bf16 v[0:15], v[224:227], v[174:177], v[0:15]
	s_cbranch_scc1 .LBB0_822
	s_add_i32 s2, s25, -7
	v_min_i32_e32 v162, s18, v188
	v_cmp_ge_i32_e32 vcc, s2, v185
	v_cmp_le_i32_e64 s[58:59], s2, v162
	s_and_b64 s[2:3], s[58:59], vcc
	s_cbranch_scc1 .Lna_inwin_0
	v_mov_b32_e32 v177, 0xf149f2ca
	v_mov_b32_e32 v176, 0xf149f2ca
	v_mov_b32_e32 v175, 0xf149f2ca
	v_mov_b32_e32 v174, 0xf149f2ca
	v_mov_b32_e32 v173, 0xf149f2ca
	v_mov_b32_e32 v172, 0xf149f2ca
	v_mov_b32_e32 v171, 0xf149f2ca
	v_mov_b32_e32 v170, 0xf149f2ca
	v_mov_b32_e32 v169, 0xf149f2ca
	v_mov_b32_e32 v168, 0xf149f2ca
	v_mov_b32_e32 v167, 0xf149f2ca
	v_mov_b32_e32 v166, 0xf149f2ca
	v_mov_b32_e32 v165, 0xf149f2ca
	v_mov_b32_e32 v164, 0xf149f2ca
	v_mov_b32_e32 v163, 0xf149f2ca
	v_mov_b32_e32 v162, 0xf149f2ca
	v_mov_b32_e32 v225, 0xf149f2ca
	v_mov_b32_e32 v222, 0xf149f2ca
	v_mov_b32_e32 v221, 0xf149f2ca
	v_mov_b32_e32 v220, 0xf149f2ca
	v_mov_b32_e32 v219, 0xf149f2ca
	v_mov_b32_e32 v218, 0xf149f2ca
	v_mov_b32_e32 v217, 0xf149f2ca
	v_mov_b32_e32 v224, 0xf149f2ca
	v_mov_b32_e32 v223, 0xf149f2ca
	v_mov_b32_e32 v216, 0xf149f2ca
	v_mov_b32_e32 v215, 0xf149f2ca
	v_mov_b32_e32 v214, 0xf149f2ca
	v_mov_b32_e32 v213, 0xf149f2ca
	v_mov_b32_e32 v212, 0xf149f2ca
	v_mov_b32_e32 v211, 0xf149f2ca
	v_mov_b32_e32 v180, 0xf149f2ca
.Lna_inwin_0:
	s_and_saveexec_b64 s[10:11], s[2:3]
	s_cbranch_execz .LBB0_821
	v_mov_b32_e32 v162, v183
	v_mov_b32_e32 v163, v182
	s_movk_i32 s2, 0xffd0
	v_lshlrev_b32_e32 v164, 2, v163
	v_max_i32_e32 v165, 8, v162
	v_lshlrev_b32_e32 v163, 4, v163
	v_lshlrev_b32_e32 v162, 2, v162
	v_sub_u32_e32 v162, v163, v162
	v_add_u32_e32 v194, v208, v162
	ds_read2_b32 v[162:163], v194 offset1:1
	v_add_u32_e32 v165, -8, v165
	v_min_u32_e32 v165, 48, v165
	v_sub_u32_e32 v195, v164, v165
	ds_read2_b32 v[164:165], v194 offset0:2 offset1:3
	ds_read2_b32 v[166:167], v194 offset0:8 offset1:9
	ds_read2_b32 v[168:169], v194 offset0:10 offset1:11
	v_add_u32_e32 v170, 1, v195
	s_waitcnt lgkmcnt(3)
	v_pk_add_f32 v[80:81], v[80:81], v[162:163]
	v_cmp_gt_u32_e32 vcc, 16, v195
	v_add_u32_e32 v171, 3, v195
	v_and_b32_e32 v196, -16, v195
	v_cndmask_b32_e32 v162, v230, v80, vcc
	v_cmp_gt_u32_e32 vcc, 16, v170
	v_add_u32_e32 v170, 2, v195
	v_add_u32_e32 v197, 34, v195
	v_cndmask_b32_e32 v163, v230, v81, vcc
	s_waitcnt lgkmcnt(2)
	v_pk_add_f32 v[80:81], v[82:83], v[164:165]
	v_cmp_gt_u32_e32 vcc, 16, v170
	v_add_u32_e32 v82, 8, v195
	v_add_u32_e32 v83, 9, v195
	v_cndmask_b32_e32 v164, v230, v80, vcc
	v_cmp_gt_u32_e32 vcc, 16, v171
	v_add_u32_e32 v171, 17, v195
	s_nop 0
	v_cndmask_b32_e32 v165, v230, v81, vcc
	s_waitcnt lgkmcnt(1)
	v_pk_add_f32 v[80:81], v[84:85], v[166:167]
	v_cmp_gt_u32_e32 vcc, 16, v82
	v_add_u32_e32 v82, 10, v195
	s_nop 0
	v_cndmask_b32_e32 v166, v230, v80, vcc
	v_cmp_gt_u32_e32 vcc, 16, v83
	v_add_u32_e32 v83, 11, v195
	s_nop 0
	v_cndmask_b32_e32 v167, v230, v81, vcc
	s_waitcnt lgkmcnt(0)
	v_pk_add_f32 v[80:81], v[86:87], v[168:169]
	v_cmp_gt_u32_e32 vcc, 16, v82
	s_nop 1
	v_cndmask_b32_e32 v168, v230, v80, vcc
	v_cmp_gt_u32_e32 vcc, 16, v83
	s_nop 1
	v_cndmask_b32_e32 v169, v230, v81, vcc
	ds_read2_b32 v[80:81], v194 offset0:16 offset1:17
	ds_read2_b32 v[82:83], v194 offset0:18 offset1:19
	ds_read2_b32 v[84:85], v194 offset0:24 offset1:25
	ds_read2_b32 v[86:87], v194 offset0:26 offset1:27
	v_cmp_lt_u32_e32 vcc, s33, v195
	s_waitcnt lgkmcnt(3)
	v_pk_add_f32 v[80:81], v[88:89], v[80:81]
	s_nop 0
	v_cndmask_b32_e32 v170, v230, v80, vcc
	v_cmp_gt_u32_e32 vcc, 16, v171
	v_add_u32_e32 v88, 18, v195
	v_add_u32_e32 v89, 19, v195
	v_cndmask_b32_e32 v171, v230, v81, vcc
	s_waitcnt lgkmcnt(2)
	v_pk_add_f32 v[80:81], v[90:91], v[82:83]
	v_cmp_gt_u32_e32 vcc, 16, v88
	v_add_u32_e32 v82, 24, v195
	v_add_u32_e32 v83, 25, v195
	v_cndmask_b32_e32 v172, v230, v80, vcc
	v_cmp_gt_u32_e32 vcc, 16, v89
	s_nop 1
	v_cndmask_b32_e32 v173, v230, v81, vcc
	s_waitcnt lgkmcnt(1)
	v_pk_add_f32 v[80:81], v[92:93], v[84:85]
	v_cmp_gt_u32_e32 vcc, 16, v82
	v_add_u32_e32 v82, 26, v195
	s_nop 0
	v_cndmask_b32_e32 v174, v230, v80, vcc
	v_cmp_gt_u32_e32 vcc, 16, v83
	v_add_u32_e32 v83, 27, v195
	s_nop 0
	v_cndmask_b32_e32 v175, v230, v81, vcc
	s_waitcnt lgkmcnt(0)
	v_pk_add_f32 v[80:81], v[94:95], v[86:87]
	v_cmp_gt_u32_e32 vcc, 16, v82
	s_nop 1
	v_cndmask_b32_e32 v176, v230, v80, vcc
	v_cmp_gt_u32_e32 vcc, 16, v83
	s_nop 1
	v_cndmask_b32_e32 v177, v230, v81, vcc
	ds_read2_b32 v[80:81], v194 offset0:32 offset1:35
	ds_read2_b32 v[82:83], v194 offset0:40 offset1:43
	ds_read2_b32 v[84:85], v194 offset0:48 offset1:51
	ds_read2_b32 v[86:87], v194 offset0:56 offset1:59
	ds_read2_b32 v[88:89], v194 offset0:33 offset1:34
	s_waitcnt lgkmcnt(4)
	v_add_f32_e32 v64, v64, v80
	v_cmp_eq_u32_e32 vcc, s84, v196
	v_add_u32_e32 v80, 33, v195
	ds_read2_b32 v[90:91], v194 offset0:41 offset1:42
	ds_read2_b32 v[92:93], v194 offset0:49 offset1:50
	ds_read2_b32 v[94:95], v194 offset0:57 offset1:58
	v_cndmask_b32_e32 v180, v230, v64, vcc
	v_mov_b32_e32 v64, v65
	v_mov_b32_e32 v65, v66
	s_waitcnt lgkmcnt(3)
	v_pk_add_f32 v[64:65], v[64:65], v[88:89]
	v_cmp_gt_u32_e32 vcc, 16, v80
	v_add_u32_e32 v80, 35, v195
	v_mov_b32_e32 v66, v81
	v_cndmask_b32_e32 v211, v230, v64, vcc
	v_cmp_gt_u32_e32 vcc, 16, v197
	v_mov_b32_e32 v64, v67
	v_mov_b32_e32 v67, v82
	v_cndmask_b32_e32 v212, v230, v65, vcc
	v_mov_b32_e32 v65, v68
	v_add_u32_e32 v88, 40, v195
	v_pk_add_f32 v[64:65], v[64:65], v[66:67]
	v_cmp_gt_u32_e32 vcc, 16, v80
	v_add_u32_e32 v66, 41, v195
	v_add_u32_e32 v67, 42, v195
	v_cndmask_b32_e32 v213, v230, v64, vcc
	v_cmp_gt_u32_e32 vcc, 16, v88
	v_mov_b32_e32 v64, v69
	v_add_u32_e32 v68, 51, v195
	v_cndmask_b32_e32 v214, v230, v65, vcc
	v_mov_b32_e32 v65, v70
	s_waitcnt lgkmcnt(2)
	v_pk_add_f32 v[64:65], v[64:65], v[90:91]
	v_cmp_gt_u32_e32 vcc, 16, v66
	v_add_u32_e32 v66, 49, v195
	v_add_u32_e32 v69, 56, v195
	v_cndmask_b32_e32 v215, v230, v64, vcc
	v_cmp_gt_u32_e32 vcc, 16, v67
	v_add_u32_e32 v64, 43, v195
	v_add_u32_e32 v67, 50, v195
	v_cndmask_b32_e32 v216, v230, v65, vcc
	v_add_f32_e32 v65, v71, v83
	v_cmp_gt_u32_e32 vcc, 16, v64
	v_add_f32_e32 v64, v72, v84
	s_nop 0
	v_cndmask_b32_e32 v223, v230, v65, vcc
	v_cmp_eq_u32_e32 vcc, s2, v196
	v_mov_b32_e32 v65, v74
	s_nop 0
	v_cndmask_b32_e32 v224, v230, v64, vcc
	v_mov_b32_e32 v64, v73
	s_waitcnt lgkmcnt(1)
	v_pk_add_f32 v[64:65], v[64:65], v[92:93]
	v_cmp_gt_u32_e32 vcc, 16, v66
	v_mov_b32_e32 v66, v85
	s_nop 0
	v_cndmask_b32_e32 v217, v230, v64, vcc
	v_cmp_gt_u32_e32 vcc, 16, v67
	v_mov_b32_e32 v64, v75
	v_mov_b32_e32 v67, v86
	v_cndmask_b32_e32 v218, v230, v65, vcc
	v_mov_b32_e32 v65, v76
	v_pk_add_f32 v[64:65], v[64:65], v[66:67]
	v_cmp_gt_u32_e32 vcc, 16, v68
	v_add_u32_e32 v66, 57, v195
	v_add_u32_e32 v67, 58, v195
	v_cndmask_b32_e32 v219, v230, v64, vcc
	v_cmp_gt_u32_e32 vcc, 16, v69
	v_mov_b32_e32 v64, v77
	s_nop 0
	v_cndmask_b32_e32 v220, v230, v65, vcc
	v_mov_b32_e32 v65, v78
	s_waitcnt lgkmcnt(0)
	v_pk_add_f32 v[64:65], v[64:65], v[94:95]
	v_cmp_gt_u32_e32 vcc, 16, v66
	s_nop 1
	v_cndmask_b32_e32 v221, v230, v64, vcc
	v_cmp_gt_u32_e32 vcc, 16, v67
	v_add_u32_e32 v64, 59, v195
	s_nop 0
	v_cndmask_b32_e32 v222, v230, v65, vcc
	v_add_f32_e32 v65, v79, v87
	v_cmp_gt_u32_e32 vcc, 16, v64
	s_nop 1
	v_cndmask_b32_e32 v225, v230, v65, vcc

.LBB0_829:
	s_ashr_i32 s3, s2, 31
	s_mul_hi_u32 s10, s2, s62
	s_mul_i32 s3, s3, s62
	s_add_i32 s3, s10, s3
	s_mul_i32 s2, s2, s62
	s_lshl_b64 s[2:3], s[2:3], 1
	s_add_u32 s10, s8, s2
	s_addc_u32 s11, s9, s3
	s_add_u32 s2, s6, s2
	s_addc_u32 s3, s7, s3
	global_load_dwordx4 v[130:133], v128, s[10:11]
	global_load_dwordx4 v[134:137], v178, s[10:11]
	global_load_dwordx4 v[138:141], v128, s[2:3]
	global_load_dwordx4 v[142:145], v178, s[2:3]
	ds_read_b64_tr_b16 v[214:215], v207 offset:0
	ds_read_b64_tr_b16 v[216:217], v207 offset:0x800
	ds_read_b64_tr_b16 v[218:219], v207 offset:0x1000
	ds_read_b64_tr_b16 v[220:221], v207 offset:0x1800
	ds_read_b64_tr_b16 v[222:223], v207 offset:0x2000
	ds_read_b64_tr_b16 v[224:225], v207 offset:0x2800
	ds_read_b64_tr_b16 v[226:227], v207 offset:0x3000
	ds_read_b64_tr_b16 v[228:229], v207 offset:0x3800
	s_waitcnt lgkmcnt(0)
	s_cmp_lt_u32 s24, 3
	v_mfma_f32_32x32x16_bf16 v[48:63], v[214:217], v[162:165], v[48:63]
	ds_read_b64_tr_b16 v[214:215], v207 offset:0x200
	ds_read_b64_tr_b16 v[216:217], v207 offset:0xa00
	v_mfma_f32_32x32x16_bf16 v[48:63], v[218:221], v[166:169], v[48:63]
	ds_read_b64_tr_b16 v[218:219], v207 offset:0x1200
	ds_read_b64_tr_b16 v[220:221], v207 offset:0x1a00
	v_mfma_f32_32x32x16_bf16 v[48:63], v[222:225], v[170:173], v[48:63]
	ds_read_b64_tr_b16 v[222:223], v207 offset:0x2200
	ds_read_b64_tr_b16 v[224:225], v207 offset:0x2a00
	v_mfma_f32_32x32x16_bf16 v[48:63], v[226:229], v[174:177], v[48:63]
	ds_read_b64_tr_b16 v[226:227], v207 offset:0x3200
	ds_read_b64_tr_b16 v[228:229], v207 offset:0x3a00
	s_waitcnt lgkmcnt(0)
	v_mfma_f32_32x32x16_bf16 v[32:47], v[214:217], v[162:165], v[32:47]
	ds_read_b64_tr_b16 v[214:215], v207 offset:0x400
	ds_read_b64_tr_b16 v[216:217], v207 offset:0xc00
	v_mfma_f32_32x32x16_bf16 v[32:47], v[218:221], v[166:169], v[32:47]
	ds_read_b64_tr_b16 v[218:219], v207 offset:0x1400
	ds_read_b64_tr_b16 v[220:221], v207 offset:0x1c00
	v_mfma_f32_32x32x16_bf16 v[32:47], v[222:225], v[170:173], v[32:47]
	ds_read_b64_tr_b16 v[222:223], v207 offset:0x2400
	ds_read_b64_tr_b16 v[224:225], v207 offset:0x2c00
	v_mfma_f32_32x32x16_bf16 v[32:47], v[226:229], v[174:177], v[32:47]
	ds_read_b64_tr_b16 v[226:227], v207 offset:0x3400
	ds_read_b64_tr_b16 v[228:229], v207 offset:0x3c00
	s_waitcnt lgkmcnt(0)
	v_mfma_f32_32x32x16_bf16 v[16:31], v[214:217], v[162:165], v[16:31]
	ds_read_b64_tr_b16 v[214:215], v207 offset:0x600
	ds_read_b64_tr_b16 v[216:217], v207 offset:0xe00
	v_mfma_f32_32x32x16_bf16 v[16:31], v[218:221], v[166:169], v[16:31]
	ds_read_b64_tr_b16 v[218:219], v207 offset:0x1600
	ds_read_b64_tr_b16 v[220:221], v207 offset:0x1e00
	v_mfma_f32_32x32x16_bf16 v[16:31], v[222:225], v[170:173], v[16:31]
	ds_read_b64_tr_b16 v[222:223], v207 offset:0x2600
	ds_read_b64_tr_b16 v[224:225], v207 offset:0x2e00
	v_mfma_f32_32x32x16_bf16 v[16:31], v[226:229], v[174:177], v[16:31]
	ds_read_b64_tr_b16 v[226:227], v207 offset:0x3600
	ds_read_b64_tr_b16 v[228:229], v207 offset:0x3e00
	s_waitcnt lgkmcnt(0)
	v_mfma_f32_32x32x16_bf16 v[0:15], v[214:217], v[162:165], v[0:15]
	v_mfma_f32_32x32x16_bf16 v[0:15], v[218:221], v[166:169], v[0:15]
	v_mfma_f32_32x32x16_bf16 v[0:15], v[222:225], v[170:173], v[0:15]
	v_mfma_f32_32x32x16_bf16 v[0:15], v[226:229], v[174:177], v[0:15]
	s_cbranch_scc1 .LBB0_833
	s_add_i32 s2, s25, -6
	v_min_i32_e32 v162, s18, v188
	v_cmp_ge_i32_e32 vcc, s2, v185
	v_cmp_le_i32_e64 s[58:59], s2, v162
	s_and_b64 s[2:3], s[58:59], vcc
	s_cbranch_scc1 .Lna_inwin_1
	v_mov_b32_e32 v220, 0xf149f2ca
	v_mov_b32_e32 v221, 0xf149f2ca
	v_mov_b32_e32 v219, 0xf149f2ca
	v_mov_b32_e32 v218, 0xf149f2ca
	v_mov_b32_e32 v217, 0xf149f2ca
	v_mov_b32_e32 v216, 0xf149f2ca
	v_mov_b32_e32 v215, 0xf149f2ca
	v_mov_b32_e32 v214, 0xf149f2ca
	v_mov_b32_e32 v211, 0xf149f2ca
	v_mov_b32_e32 v177, 0xf149f2ca
	v_mov_b32_e32 v176, 0xf149f2ca
	v_mov_b32_e32 v175, 0xf149f2ca
	v_mov_b32_e32 v174, 0xf149f2ca
	v_mov_b32_e32 v173, 0xf149f2ca
	v_mov_b32_e32 v172, 0xf149f2ca
	v_mov_b32_e32 v163, 0xf149f2ca
	v_mov_b32_e32 v228, 0xf149f2ca
	v_mov_b32_e32 v227, 0xf149f2ca
	v_mov_b32_e32 v171, 0xf149f2ca
	v_mov_b32_e32 v170, 0xf149f2ca
	v_mov_b32_e32 v169, 0xf149f2ca
	v_mov_b32_e32 v168, 0xf149f2ca
	v_mov_b32_e32 v226, 0xf149f2ca
	v_mov_b32_e32 v225, 0xf149f2ca
	v_mov_b32_e32 v224, 0xf149f2ca
	v_mov_b32_e32 v223, 0xf149f2ca
	v_mov_b32_e32 v167, 0xf149f2ca
	v_mov_b32_e32 v166, 0xf149f2ca
	v_mov_b32_e32 v165, 0xf149f2ca
	v_mov_b32_e32 v164, 0xf149f2ca
	v_mov_b32_e32 v222, 0xf149f2ca
	v_mov_b32_e32 v162, 0xf149f2ca
.Lna_inwin_1:
	s_and_saveexec_b64 s[10:11], s[2:3]
	s_cbranch_execz .LBB0_832
	v_mov_b32_e32 v162, v183
	v_mov_b32_e32 v163, v182
	s_movk_i32 s2, 0xffd0
	v_lshlrev_b32_e32 v164, 2, v163
	v_max_i32_e32 v165, 8, v162
	v_lshlrev_b32_e32 v163, 4, v163
	v_lshlrev_b32_e32 v162, 2, v162
	v_sub_u32_e32 v162, v163, v162
	v_add_u32_e32 v170, v208, v162
	ds_read2_b32 v[162:163], v170 offset0:31 offset1:32
	v_add_u32_e32 v165, -8, v165
	v_min_u32_e32 v165, 48, v165
	v_sub_u32_e32 v194, v164, v165
	ds_read2_b32 v[164:165], v170 offset0:33 offset1:34
	ds_read2_b32 v[166:167], v170 offset0:39 offset1:40
	ds_read2_b32 v[168:169], v170 offset0:41 offset1:42
	v_add_u32_e32 v171, 1, v194
	s_waitcnt lgkmcnt(3)
	v_pk_add_f32 v[80:81], v[80:81], v[162:163]
	v_cmp_gt_u32_e32 vcc, 16, v194
	v_add_u32_e32 v162, 2, v194
	s_nop 0
	v_cndmask_b32_e32 v163, v230, v80, vcc
	v_cmp_gt_u32_e32 vcc, 16, v171
	v_add_u32_e32 v171, 3, v194
	s_nop 0
	v_cndmask_b32_e32 v172, v230, v81, vcc
	s_waitcnt lgkmcnt(2)
	v_pk_add_f32 v[80:81], v[82:83], v[164:165]
	v_cmp_gt_u32_e32 vcc, 16, v162
	v_add_u32_e32 v82, 8, v194
	v_add_u32_e32 v83, 9, v194
	v_cndmask_b32_e32 v173, v230, v80, vcc
	v_cmp_gt_u32_e32 vcc, 16, v171
	v_add_u32_e32 v162, 17, v194
	v_add_u32_e32 v164, 34, v194
	v_cndmask_b32_e32 v174, v230, v81, vcc
	s_waitcnt lgkmcnt(1)
	v_pk_add_f32 v[80:81], v[84:85], v[166:167]
	v_cmp_gt_u32_e32 vcc, 16, v82
	v_add_u32_e32 v82, 10, v194
	s_nop 0
	v_cndmask_b32_e32 v175, v230, v80, vcc
	v_cmp_gt_u32_e32 vcc, 16, v83
	v_add_u32_e32 v83, 11, v194
	s_nop 0
	v_cndmask_b32_e32 v176, v230, v81, vcc
	s_waitcnt lgkmcnt(0)
	v_pk_add_f32 v[80:81], v[86:87], v[168:169]
	v_cmp_gt_u32_e32 vcc, 16, v82
	v_and_b32_e32 v168, -16, v194
	s_nop 0
	v_cndmask_b32_e32 v177, v230, v80, vcc
	v_cmp_gt_u32_e32 vcc, 16, v83
	s_nop 1
	v_cndmask_b32_e32 v211, v230, v81, vcc
	ds_read2_b32 v[80:81], v170 offset0:47 offset1:48
	ds_read2_b32 v[82:83], v170 offset0:49 offset1:50
	ds_read2_b32 v[84:85], v170 offset0:55 offset1:56
	ds_read2_b32 v[86:87], v170 offset0:57 offset1:58
	v_cmp_lt_u32_e32 vcc, s33, v194
	s_waitcnt lgkmcnt(3)
	v_pk_add_f32 v[80:81], v[88:89], v[80:81]
	s_nop 0
	v_cndmask_b32_e32 v214, v230, v80, vcc
	v_cmp_gt_u32_e32 vcc, 16, v162
	v_add_u32_e32 v88, 18, v194
	v_add_u32_e32 v89, 19, v194
	v_cndmask_b32_e32 v215, v230, v81, vcc
	s_waitcnt lgkmcnt(2)
	v_pk_add_f32 v[80:81], v[90:91], v[82:83]
	v_cmp_gt_u32_e32 vcc, 16, v88
	v_add_u32_e32 v82, 24, v194
	v_add_u32_e32 v83, 25, v194
	v_cndmask_b32_e32 v216, v230, v80, vcc
	v_cmp_gt_u32_e32 vcc, 16, v89
	s_nop 1
	v_cndmask_b32_e32 v217, v230, v81, vcc
	s_waitcnt lgkmcnt(1)
	v_pk_add_f32 v[80:81], v[92:93], v[84:85]
	v_cmp_gt_u32_e32 vcc, 16, v82
	v_add_u32_e32 v82, 26, v194
	s_nop 0
	v_cndmask_b32_e32 v218, v230, v80, vcc
	v_cmp_gt_u32_e32 vcc, 16, v83
	v_add_u32_e32 v83, 27, v194
	s_nop 0
	v_cndmask_b32_e32 v219, v230, v81, vcc
	s_waitcnt lgkmcnt(0)
	v_pk_add_f32 v[80:81], v[94:95], v[86:87]
	v_cmp_gt_u32_e32 vcc, 16, v82
	s_nop 1
	v_cndmask_b32_e32 v221, v230, v80, vcc
	v_cmp_gt_u32_e32 vcc, 16, v83
	s_nop 1
	v_cndmask_b32_e32 v220, v230, v81, vcc
	ds_read2_b32 v[80:81], v170 offset0:63 offset1:66
	ds_read2_b32 v[82:83], v170 offset0:71 offset1:74
	ds_read2_b32 v[84:85], v170 offset0:79 offset1:82
	ds_read2_b32 v[86:87], v170 offset0:87 offset1:90
	ds_read2_b32 v[88:89], v170 offset0:64 offset1:65
	s_waitcnt lgkmcnt(4)
	v_add_f32_e32 v64, v64, v80
	v_cmp_eq_u32_e32 vcc, s84, v168
	v_add_u32_e32 v80, 33, v194
	ds_read2_b32 v[90:91], v170 offset0:72 offset1:73
	ds_read2_b32 v[92:93], v170 offset0:80 offset1:81
	ds_read2_b32 v[94:95], v170 offset0:88 offset1:89
	v_cndmask_b32_e32 v162, v230, v64, vcc
	v_mov_b32_e32 v64, v65
	v_mov_b32_e32 v65, v66
	s_waitcnt lgkmcnt(3)
	v_pk_add_f32 v[64:65], v[64:65], v[88:89]
	v_cmp_gt_u32_e32 vcc, 16, v80
	v_add_u32_e32 v80, 35, v194
	v_mov_b32_e32 v66, v81
	v_cndmask_b32_e32 v222, v230, v64, vcc
	v_cmp_gt_u32_e32 vcc, 16, v164
	v_mov_b32_e32 v64, v67
	v_mov_b32_e32 v67, v82
	v_cndmask_b32_e32 v164, v230, v65, vcc
	v_mov_b32_e32 v65, v68
	v_add_u32_e32 v88, 40, v194
	v_pk_add_f32 v[64:65], v[64:65], v[66:67]
	v_cmp_gt_u32_e32 vcc, 16, v80
	v_add_u32_e32 v66, 41, v194
	v_add_u32_e32 v67, 42, v194
	v_cndmask_b32_e32 v165, v230, v64, vcc
	v_cmp_gt_u32_e32 vcc, 16, v88
	v_mov_b32_e32 v64, v69
	v_add_u32_e32 v68, 51, v194
	v_cndmask_b32_e32 v166, v230, v65, vcc
	v_mov_b32_e32 v65, v70
	s_waitcnt lgkmcnt(2)
	v_pk_add_f32 v[64:65], v[64:65], v[90:91]
	v_cmp_gt_u32_e32 vcc, 16, v66
	v_add_u32_e32 v66, 49, v194
	v_add_u32_e32 v69, 56, v194
	v_cndmask_b32_e32 v167, v230, v64, vcc
	v_cmp_gt_u32_e32 vcc, 16, v67
	v_add_u32_e32 v64, 43, v194
	v_add_u32_e32 v67, 50, v194
	v_cndmask_b32_e32 v223, v230, v65, vcc
	v_add_f32_e32 v65, v71, v83
	v_cmp_gt_u32_e32 vcc, 16, v64
	v_add_f32_e32 v64, v72, v84
	s_nop 0
	v_cndmask_b32_e32 v224, v230, v65, vcc
	v_cmp_eq_u32_e32 vcc, s2, v168
	v_mov_b32_e32 v65, v74
	s_nop 0
	v_cndmask_b32_e32 v225, v230, v64, vcc
	v_mov_b32_e32 v64, v73
	s_waitcnt lgkmcnt(1)
	v_pk_add_f32 v[64:65], v[64:65], v[92:93]
	v_cmp_gt_u32_e32 vcc, 16, v66
	v_mov_b32_e32 v66, v85
	s_nop 0
	v_cndmask_b32_e32 v226, v230, v64, vcc
	v_cmp_gt_u32_e32 vcc, 16, v67
	v_mov_b32_e32 v64, v75
	v_mov_b32_e32 v67, v86
	v_cndmask_b32_e32 v168, v230, v65, vcc
	v_mov_b32_e32 v65, v76
	v_pk_add_f32 v[64:65], v[64:65], v[66:67]
	v_cmp_gt_u32_e32 vcc, 16, v68
	v_add_u32_e32 v66, 57, v194
	v_add_u32_e32 v67, 58, v194
	v_cndmask_b32_e32 v169, v230, v64, vcc
	v_cmp_gt_u32_e32 vcc, 16, v69
	v_mov_b32_e32 v64, v77
	s_nop 0
	v_cndmask_b32_e32 v170, v230, v65, vcc
	v_mov_b32_e32 v65, v78
	s_waitcnt lgkmcnt(0)
	v_pk_add_f32 v[64:65], v[64:65], v[94:95]
	v_cmp_gt_u32_e32 vcc, 16, v66
	s_nop 1
	v_cndmask_b32_e32 v171, v230, v64, vcc
	v_cmp_gt_u32_e32 vcc, 16, v67
	v_add_u32_e32 v64, 59, v194
	s_nop 0
	v_cndmask_b32_e32 v227, v230, v65, vcc
	v_add_f32_e32 v65, v79, v87
	v_cmp_gt_u32_e32 vcc, 16, v64
	s_nop 1
	v_cndmask_b32_e32 v228, v230, v65, vcc
